# baseline (speedup 1.0000x reference)
.LBB1_31:
	s_waitcnt vmcnt(6)
	v_mbcnt_lo_u32_b32 v64, -1, 0
	v_mbcnt_hi_u32_b32 v100, -1, v64
	s_andn2_b32 s25, s25, 63
	v_add_u32_e32 v64, s25, v100
	v_ashrrev_i32_e32 v64, 4, v64
	s_movk_i32 s0, 0x44
	v_and_b32_e32 v101, 15, v100
	v_mul_lo_u32 v64, v64, s0
	v_lshl_add_u32 v64, v101, 2, v64
	s_and_b64 vcc, exec, s[8:9]
	s_barrier
	ds_write_b32 v64, v104
	ds_write_b32 v64, v105 offset:1360
	ds_write_b32 v64, v106 offset:2720
	ds_write_b32 v64, v107 offset:4080
	s_waitcnt lgkmcnt(0)
	s_barrier
	s_cbranch_vccz .LBB1_38
	v_and_b32_e32 v64, 3, v100
	v_and_b32_e32 v65, 0x7c, v100
	s_movk_i32 s0, 0x550
	v_mad_u32_u24 v70, v64, s0, v65
	ds_read2_b32 v[72:73], v70 offset1:17
	ds_read2_b32 v[74:75], v70 offset0:34 offset1:51
	ds_read2_b32 v[76:77], v70 offset0:68 offset1:85
	ds_read2_b32 v[78:79], v70 offset0:102 offset1:119
	ds_read2_b32 v[80:81], v70 offset0:136 offset1:153
	ds_read2_b32 v[82:83], v70 offset0:170 offset1:187
	ds_read2_b32 v[84:85], v70 offset0:204 offset1:221
	ds_read2_b32 v[86:87], v70 offset0:238 offset1:255
	v_add_u32_e32 v71, 0x400, v70
	ds_read2_b32 v[88:89], v71 offset0:16 offset1:33
	ds_read2_b32 v[90:91], v71 offset0:50 offset1:67
	s_mov_b32 s0, 0xf800000
	s_lshl_b32 s10, s23, 8
	s_waitcnt lgkmcnt(0)
	v_add_f32_e32 v64, 0, v72
	v_add_f32_e32 v64, v64, v73
	v_add_f32_e32 v64, v64, v74
	v_add_f32_e32 v64, v64, v75
	v_add_f32_e32 v64, v64, v76
	v_add_f32_e32 v64, v64, v77
	v_add_f32_e32 v64, v64, v78
	v_add_f32_e32 v64, v64, v79
	v_add_f32_e32 v64, v64, v80
	v_add_f32_e32 v64, v64, v81
	v_add_f32_e32 v64, v64, v82
	v_add_f32_e32 v64, v64, v83
	v_add_f32_e32 v64, v64, v84
	v_add_f32_e32 v64, v64, v85
	v_add_f32_e32 v64, v64, v86
	v_add_f32_e32 v64, v64, v87
	v_add_f32_e32 v64, v64, v88
	v_add_f32_e32 v64, v64, v89
	v_add_f32_e32 v64, v64, v90
	v_add_f32_e32 v64, v64, v91
	v_mul_f32_e32 v65, 0x4f800000, v64
	v_cmp_gt_f32_e32 vcc, s0, v64
	v_mov_b32_e32 v70, v58
	v_mov_b32_e32 v71, v50
	v_cndmask_b32_e32 v64, v64, v65, vcc
	v_sqrt_f32_e32 v65, v64
	s_waitcnt vmcnt(0)
	s_mul_i32 s16, s24, 0x1400
	s_add_u32 s16, s6, s16
	s_addc_u32 s17, s7, 0
	s_add_u32 s18, s16, 0x1000
	s_addc_u32 s19, s17, 0
	v_lshlrev_b32_e32 v122, 2, v100
	global_load_dword v103, v122, s[16:17]
	global_load_dword v104, v122, s[16:17] offset:256
	global_load_dword v105, v122, s[16:17] offset:512
	global_load_dword v106, v122, s[16:17] offset:768
	global_load_dword v107, v122, s[16:17] offset:1024
	global_load_dword v108, v122, s[16:17] offset:1280
	global_load_dword v109, v122, s[16:17] offset:1536
	global_load_dword v110, v122, s[16:17] offset:1792
	global_load_dword v111, v122, s[16:17] offset:2048
	global_load_dword v112, v122, s[16:17] offset:2304
	global_load_dword v113, v122, s[16:17] offset:2560
	global_load_dword v114, v122, s[16:17] offset:2816
	global_load_dword v115, v122, s[16:17] offset:3072
	global_load_dword v116, v122, s[16:17] offset:3328
	global_load_dword v117, v122, s[16:17] offset:3584
	global_load_dword v118, v122, s[16:17] offset:3840
	global_load_dword v119, v122, s[18:19]
	global_load_dword v120, v122, s[18:19] offset:256
	global_load_dword v121, v122, s[18:19] offset:512
	global_load_dword v122, v122, s[18:19] offset:768
	v_mov_b32_e32 v72, v59
	v_mov_b32_e32 v73, v51
	v_mov_b32_e32 v74, v41
	v_add_u32_e32 v66, -1, v65
	v_fma_f32 v67, -v66, v65, v64
	v_cmp_ge_f32_e64 s[0:1], 0, v67
	v_add_u32_e32 v67, 1, v65
	v_mov_b32_e32 v75, v33
	v_cndmask_b32_e64 v66, v65, v66, s[0:1]
	v_fma_f32 v65, -v67, v65, v64
	v_cmp_lt_f32_e64 s[0:1], 0, v65
	v_mov_b32_e32 v76, v43
	v_mov_b32_e32 v77, v35
	v_cndmask_b32_e64 v65, v66, v67, s[0:1]
	v_mul_f32_e32 v66, 0x37800000, v65
	v_cndmask_b32_e32 v65, v65, v66, vcc
	v_mov_b32_e32 v66, 0x260
	v_cmp_class_f32_e32 vcc, v64, v66
	v_mov_b32_e32 v78, v25
	v_mov_b32_e32 v79, v17
	v_cndmask_b32_e32 v64, v65, v64, vcc
	v_add_f32_e32 v64, 0x322bcc77, v64
	v_div_scale_f32 v65, s[0:1], v64, v64, 1.0
	v_rcp_f32_e32 v66, v65
	s_mul_i32 s0, s23, 0x180
	s_add_i32 s8, s10, s0
	s_mov_b32 s0, 0x3a83126f
	v_fma_f32 v67, -v65, v66, 1.0
	v_fmac_f32_e32 v66, v67, v66
	v_div_scale_f32 v67, vcc, 1.0, v64, 1.0
	v_mul_f32_e32 v68, v67, v66
	v_fma_f32 v69, -v65, v68, v67
	v_fmac_f32_e32 v68, v69, v66
	v_fma_f32 v65, -v65, v68, v67
	v_div_fmas_f32 v65, v65, v66, v68
	v_div_fixup_f32 v64, v65, v64, 1.0
	v_lshl_add_u32 v65, v100, 2, s10
	ds_write_b32 v65, v64 offset:8832
	v_add_f32_e32 v80, v60, v56
	v_add_f32_e32 v81, v52, v48
	v_add_f32_e32 v64, v80, v81
	v_add_f32_e32 v82, v61, v57
	v_add_f32_e32 v83, v53, v49
	v_add_f32_e32 v65, v82, v83
	v_add_f32_e32 v80, v62, v58
	v_add_f32_e32 v81, v54, v50
	v_add_f32_e32 v66, v80, v81
	v_add_f32_e32 v82, v63, v59
	v_add_f32_e32 v83, v55, v51
	v_add_f32_e32 v67, v82, v83
	v_add_f32_e32 v80, v44, v40
	v_add_f32_e32 v81, v36, v32
	v_add_f32_e32 v68, v80, v81
	v_add_f32_e32 v82, v45, v41
	v_add_f32_e32 v83, v37, v33
	v_add_f32_e32 v69, v82, v83
	v_add_f32_e32 v80, v46, v42
	v_add_f32_e32 v81, v38, v34
	v_add_f32_e32 v70, v80, v81
	v_add_f32_e32 v82, v47, v43
	v_add_f32_e32 v83, v39, v35
	v_add_f32_e32 v71, v82, v83
	v_add_f32_e32 v80, v28, v24
	v_add_f32_e32 v81, v20, v16
	v_add_f32_e32 v72, v80, v81
	v_add_f32_e32 v82, v29, v25
	v_add_f32_e32 v83, v21, v17
	v_add_f32_e32 v73, v82, v83
	v_add_f32_e32 v80, v30, v26
	v_add_f32_e32 v81, v22, v18
	v_add_f32_e32 v74, v80, v81
	v_add_f32_e32 v82, v31, v27
	v_add_f32_e32 v83, v23, v19
	v_add_f32_e32 v75, v82, v83
	v_add_f32_e32 v80, v12, v8
	v_add_f32_e32 v81, v4, v0
	v_add_f32_e32 v76, v80, v81
	v_add_f32_e32 v82, v13, v9
	v_add_f32_e32 v83, v5, v1
	v_add_f32_e32 v77, v82, v83
	v_add_f32_e32 v80, v14, v10
	v_add_f32_e32 v81, v6, v2
	v_add_f32_e32 v78, v80, v81
	v_add_f32_e32 v82, v15, v11
	v_add_f32_e32 v83, v7, v3
	v_add_f32_e32 v79, v82, v83
	v_add_f32_dpp v84, v64, v64 row_ror:8 row_mask:0xf bank_mask:0x3
	v_add_f32_dpp v84, v72, v72 row_ror:8 row_mask:0xf bank_mask:0xc
	v_add_f32_dpp v85, v65, v65 row_ror:8 row_mask:0xf bank_mask:0x3
	v_add_f32_dpp v85, v73, v73 row_ror:8 row_mask:0xf bank_mask:0xc
	v_add_f32_dpp v86, v66, v66 row_ror:8 row_mask:0xf bank_mask:0x3
	v_add_f32_dpp v86, v74, v74 row_ror:8 row_mask:0xf bank_mask:0xc
	v_add_f32_dpp v87, v67, v67 row_ror:8 row_mask:0xf bank_mask:0x3
	v_add_f32_dpp v87, v75, v75 row_ror:8 row_mask:0xf bank_mask:0xc
	v_add_f32_dpp v88, v68, v68 row_ror:8 row_mask:0xf bank_mask:0x3
	v_add_f32_dpp v88, v76, v76 row_ror:8 row_mask:0xf bank_mask:0xc
	v_add_f32_dpp v89, v69, v69 row_ror:8 row_mask:0xf bank_mask:0x3
	v_add_f32_dpp v89, v77, v77 row_ror:8 row_mask:0xf bank_mask:0xc
	v_add_f32_dpp v90, v70, v70 row_ror:8 row_mask:0xf bank_mask:0x3
	v_add_f32_dpp v90, v78, v78 row_ror:8 row_mask:0xf bank_mask:0xc
	v_add_f32_dpp v91, v71, v71 row_ror:8 row_mask:0xf bank_mask:0x3
	v_add_f32_dpp v91, v79, v79 row_ror:8 row_mask:0xf bank_mask:0xc
	v_add_f32_dpp v92, v84, v84 row_ror:12 row_mask:0xf bank_mask:0x5
	v_add_f32_dpp v92, v88, v88 row_ror:4 row_mask:0xf bank_mask:0xa
	v_add_f32_dpp v93, v85, v85 row_ror:12 row_mask:0xf bank_mask:0x5
	v_add_f32_dpp v93, v89, v89 row_ror:4 row_mask:0xf bank_mask:0xa
	v_add_f32_dpp v94, v86, v86 row_ror:12 row_mask:0xf bank_mask:0x5
	v_add_f32_dpp v94, v90, v90 row_ror:4 row_mask:0xf bank_mask:0xa
	v_add_f32_dpp v95, v87, v87 row_ror:12 row_mask:0xf bank_mask:0x5
	v_add_f32_dpp v95, v91, v91 row_ror:4 row_mask:0xf bank_mask:0xa
	v_add_f32_dpp v92, v92, v92 quad_perm:[2,3,0,1] row_mask:0xf bank_mask:0xf
	v_add_f32_dpp v93, v93, v93 quad_perm:[2,3,0,1] row_mask:0xf bank_mask:0xf
	v_add_f32_dpp v94, v94, v94 quad_perm:[2,3,0,1] row_mask:0xf bank_mask:0xf
	v_add_f32_dpp v95, v95, v95 quad_perm:[2,3,0,1] row_mask:0xf bank_mask:0xf
	v_add_f32_dpp v92, v92, v92 quad_perm:[1,0,3,2] row_mask:0xf bank_mask:0xf
	v_add_f32_dpp v93, v93, v93 quad_perm:[1,0,3,2] row_mask:0xf bank_mask:0xf
	v_add_f32_dpp v94, v94, v94 quad_perm:[1,0,3,2] row_mask:0xf bank_mask:0xf
	v_add_f32_dpp v95, v95, v95 quad_perm:[1,0,3,2] row_mask:0xf bank_mask:0xf
	v_mul_f32_e32 v92, 0x3c800000, v92
	v_mul_f32_e32 v93, 0x3c800000, v93
	v_mul_f32_e32 v94, 0x3c800000, v94
	v_mul_f32_e32 v95, 0x3c800000, v95
	v_max_f32_e32 v92, 0, v92
	v_max_f32_e32 v93, 0, v93
	v_max_f32_e32 v94, 0, v94
	v_max_f32_e32 v95, 0, v95
	v_add_f32_e32 v92, 0x3a83126f, v92
	v_add_f32_e32 v93, 0x3a83126f, v93
	v_add_f32_e32 v94, 0x3a83126f, v94
	v_add_f32_e32 v95, 0x3a83126f, v95
	v_add_f32_e32 v96, v92, v93
	v_add_f32_e32 v96, v96, v94
	v_add_f32_e32 v96, v96, v95
	v_add_f32_dpp v96, v92, v96 row_ror:12 row_mask:0xf bank_mask:0xf
	v_add_f32_dpp v96, v93, v96 row_ror:12 row_mask:0xf bank_mask:0xf
	v_add_f32_dpp v96, v94, v96 row_ror:12 row_mask:0xf bank_mask:0xf
	v_add_f32_dpp v96, v95, v96 row_ror:12 row_mask:0xf bank_mask:0xf
	v_add_f32_dpp v96, v92, v96 row_ror:8 row_mask:0xf bank_mask:0xf
	v_add_f32_dpp v96, v93, v96 row_ror:8 row_mask:0xf bank_mask:0xf
	v_add_f32_dpp v96, v94, v96 row_ror:8 row_mask:0xf bank_mask:0xf
	v_add_f32_dpp v96, v95, v96 row_ror:8 row_mask:0xf bank_mask:0xf
	v_add_f32_dpp v96, v92, v96 row_ror:4 row_mask:0xf bank_mask:0xf
	v_add_f32_dpp v96, v93, v96 row_ror:4 row_mask:0xf bank_mask:0xf
	v_add_f32_dpp v96, v94, v96 row_ror:4 row_mask:0xf bank_mask:0xf
	v_add_f32_dpp v96, v95, v96 row_ror:4 row_mask:0xf bank_mask:0xf
	v_mov_b32_e32 v97, v96
	s_nop 1
	v_permlane16_swap_b32_e32 v96, v97
	v_add_f32_e32 v96, v96, v97
	v_mov_b32_e32 v97, v96
	s_nop 1
	v_permlane32_swap_b32_e32 v96, v97
	v_add_f32_e32 v96, v96, v97
	s_nop 0
	v_readfirstlane_b32 s2, v96
	v_and_b32_e32 v99, 3, v100
	v_lshlrev_b32_e32 v98, 4, v101
	v_mov_b32_e32 v80, s2
	v_div_scale_f32 v81, s[2:3], v80, v80, 1.0
	v_rcp_f32_e32 v82, v81
	v_div_scale_f32 v83, vcc, 1.0, v80, 1.0
	v_fma_f32 v84, -v81, v82, 1.0
	v_fmac_f32_e32 v82, v84, v82
	v_mul_f32_e32 v84, v83, v82
	v_fma_f32 v85, -v81, v84, v83
	v_fmac_f32_e32 v84, v85, v82
	v_fma_f32 v81, -v81, v84, v83
	v_div_fmas_f32 v81, v81, v82, v84
	v_div_fixup_f32 v80, v81, v80, 1.0
	v_mul_f32_e32 v92, v80, v92
	v_mul_f32_e32 v93, v80, v93
	v_mul_f32_e32 v94, v80, v94
	v_mul_f32_e32 v95, v80, v95
	v_and_b32_e32 v97, 48, v100
	v_add3_u32 v98, v98, v97, s8
	v_cmp_eq_u32_e32 vcc, 0, v99
	s_and_saveexec_b64 s[2:3], vcc
	ds_write_b128 v98, v[92:95] offset:5632
	s_mov_b64 exec, s[2:3]
	v_add_f32_e32 v64, v60, v61
	v_add_f32_e32 v65, v62, v63
	v_add_f32_e32 v64, v64, v65
	v_add_f32_e32 v65, v44, v45
	v_add_f32_e32 v66, v46, v47
	v_add_f32_e32 v64, 0, v64
	v_add_f32_e32 v65, v65, v66
	v_add_f32_e32 v64, v64, v65
	v_add_f32_e32 v65, v28, v29
	v_add_f32_e32 v66, v30, v31
	v_add_f32_e32 v65, v65, v66
	v_add_f32_e32 v64, v64, v65
	v_add_f32_e32 v65, v12, v13
	v_add_f32_e32 v66, v14, v15
	v_add_f32_e32 v65, v65, v66
	v_add_f32_e32 v64, v64, v65
	v_mov_b32_e32 v65, v64
	s_nop 1
	v_permlane16_swap_b32_e32 v64, v65
	v_add_f32_e32 v64, v64, v65
	v_mov_b32_e32 v65, v64
	s_nop 1
	v_permlane32_swap_b32_e32 v64, v65
	v_add_f32_e32 v64, v64, v65
	v_add_f32_e32 v65, v56, v57
	v_add_f32_e32 v66, v58, v59
	v_add_f32_e32 v65, v65, v66
	v_add_f32_e32 v66, v40, v41
	v_add_f32_e32 v67, v42, v43
	v_add_f32_e32 v65, 0, v65
	v_add_f32_e32 v66, v66, v67
	v_add_f32_e32 v65, v65, v66
	v_add_f32_e32 v66, v24, v25
	v_add_f32_e32 v67, v26, v27
	v_add_f32_e32 v66, v66, v67
	v_add_f32_e32 v65, v65, v66
	v_add_f32_e32 v66, v8, v9
	v_add_f32_e32 v67, v10, v11
	v_add_f32_e32 v66, v66, v67
	v_add_f32_e32 v65, v65, v66
	v_mov_b32_e32 v66, v65
	s_nop 1
	v_permlane16_swap_b32_e32 v65, v66
	v_add_f32_e32 v65, v65, v66
	v_mov_b32_e32 v66, v65
	s_nop 1
	v_permlane32_swap_b32_e32 v65, v66
	v_add_f32_e32 v65, v65, v66
	v_add_f32_e32 v66, v52, v53
	v_add_f32_e32 v68, v54, v55
	v_add_f32_e32 v66, v66, v68
	v_add_f32_e32 v68, v36, v37
	v_add_f32_e32 v69, v38, v39
	v_add_f32_e32 v66, 0, v66
	v_add_f32_e32 v68, v68, v69
	v_add_f32_e32 v66, v66, v68
	v_add_f32_e32 v68, v20, v21
	v_add_f32_e32 v69, v22, v23
	v_add_f32_e32 v68, v68, v69
	v_add_f32_e32 v66, v66, v68
	v_add_f32_e32 v68, v4, v5
	v_add_f32_e32 v69, v6, v7
	v_add_f32_e32 v68, v68, v69
	v_add_f32_e32 v66, v66, v68
	v_mov_b32_e32 v68, v66
	s_nop 1
	v_permlane16_swap_b32_e32 v66, v68
	v_add_f32_e32 v66, v66, v68
	v_mov_b32_e32 v68, v66
	s_nop 1
	v_permlane32_swap_b32_e32 v66, v68
	v_mul_f32_e32 v64, 0x3c800000, v64
	v_mul_f32_e32 v65, 0x3c800000, v65
	v_add_f32_e32 v66, v66, v68
	v_max_f32_e32 v64, 0, v64
	v_max_f32_e32 v65, 0, v65
	v_mul_f32_e32 v66, 0x3c800000, v66
	v_add_f32_e32 v64, 0x3a83126f, v64
	v_add_f32_e32 v65, 0x3a83126f, v65
	v_max_f32_e32 v66, 0, v66
	v_add_f32_e32 v67, v64, v65
	v_add_f32_e32 v66, 0x3a83126f, v66
	v_add_f32_e32 v68, v67, v66
	v_add_f32_e32 v67, v48, v49
	v_add_f32_e32 v69, v50, v51
	v_add_f32_e32 v67, v67, v69
	v_add_f32_e32 v69, v32, v33
	v_add_f32_e32 v70, v34, v35
	v_add_f32_e32 v67, 0, v67
	v_add_f32_e32 v69, v69, v70
	v_add_f32_e32 v67, v67, v69
	v_add_f32_e32 v69, v16, v17
	v_add_f32_e32 v70, v18, v19
	v_add_f32_e32 v69, v69, v70
	v_add_f32_e32 v67, v67, v69
	v_add_f32_e32 v69, v0, v1
	v_add_f32_e32 v70, v2, v3
	v_add_f32_e32 v69, v69, v70
	v_add_f32_e32 v67, v67, v69
	v_mov_b32_e32 v69, v67
	s_nop 1
	v_permlane16_swap_b32_e32 v67, v69
	v_add_f32_e32 v67, v67, v69
	v_mov_b32_e32 v69, v67
	s_nop 1
	v_permlane32_swap_b32_e32 v67, v69
	v_add_f32_e32 v67, v67, v69
	v_mul_f32_e32 v67, 0x3c800000, v67
	v_max_f32_e32 v67, 0, v67
	v_add_f32_e32 v67, 0x3a83126f, v67
	v_add_f32_e32 v68, v68, v67
	s_mov_b32 s9, 0
	v_cmp_gt_u32_e64 s[0:1], 16, v100
	v_add_f32_dpp v68, v68, v68 row_ror:8 row_mask:0xf bank_mask:0xf bound_ctrl:1
	v_lshl_add_u32 v102, v100, 2, s8
	s_nop 0
	v_add_f32_dpp v68, v68, v68 row_ror:4 row_mask:0xf bank_mask:0xf bound_ctrl:1
	s_nop 1
	v_add_f32_dpp v68, v68, v68 row_ror:2 row_mask:0xf bank_mask:0xf bound_ctrl:1
	s_nop 1
	v_mov_b32_dpp v69, v68 row_ror:1 row_mask:0xf bank_mask:0xf bound_ctrl:1
	s_and_saveexec_b64 s[2:3], s[0:1]
	s_cbranch_execz .LBB1_36
	v_add_f32_e32 v68, v68, v69
	v_div_scale_f32 v69, s[4:5], v68, v68, 1.0
	v_rcp_f32_e32 v70, v69
	v_div_scale_f32 v71, vcc, 1.0, v68, 1.0
	v_fma_f32 v72, -v69, v70, 1.0
	v_fmac_f32_e32 v70, v72, v70
	v_mul_f32_e32 v72, v71, v70
	v_fma_f32 v73, -v69, v72, v71
	v_fmac_f32_e32 v72, v73, v70
	v_fma_f32 v69, -v69, v72, v71
	v_div_fmas_f32 v69, v69, v70, v72
	v_div_fixup_f32 v68, v69, v68, 1.0
	v_mul_f32_e32 v64, v68, v64
	v_mul_f32_e32 v65, v68, v65
	v_add_u32_e32 v69, 0x1400, v102
	ds_write2_b32 v69, v64, v65 offset0:192 offset1:208
	v_mul_f32_e32 v64, v68, v66
	v_mul_f32_e32 v65, v68, v67
	ds_write2_b32 v69, v64, v65 offset0:224 offset1:240
